# v23 + static s_setprio 1 for waves 0-3 (instead of 4-7) during P3
# baseline (speedup 1.0000x reference)
; __device__ __forceinline__ void p3_attention(Frame& F) {
;     const int c = blockIdx.x; if (c >= 256) return;
;     const int xcd = c & 7, j = c >> 3, bh = xcd * 2 + (j >> 4), qb = j & 15, b = bh >> 3, h = bh & 7;
;     const bf16_t* KV = (const bf16_t*)(F.ws + WS_KV);
;     f32x16 o[4];
;     const int tid = F.tid, wid = tid >> 6, lane = tid & 63, r32 = lane & 31, hi = lane >> 5;
.LBB0_408:
	s_cmp_lt_i32 s34, 4
	s_cselect_b64 s[16:17], -1, 0
	s_cmpk_lt_i32 s2, 0x100
	s_cselect_b64 s[12:13], -1, 0
	s_and_b64 s[0:1], s[12:13], s[0:1]
	s_and_b64 s[0:1], s[16:17], s[0:1]
	s_andn2_b64 vcc, exec, s[0:1]
	s_cbranch_vccnz .LBB0_492
	v_readlane_b32 s99, v255, 8
	s_nop 3
	s_cmp_lt_u32 s99, 4
	s_cbranch_scc0 .Lp3_prio_done
	s_setprio 1
